# speedup vs baseline: 1.0143x; 1.0017x over previous
.Lm_nok_p1:
	s_waitcnt vmcnt(2)
	s_nop 0
	v_max3_f32 v132, v132, v133, v134
	v_max3_f32 v136, v136, v137, v138
	v_max3_f32 v132, v132, v135, v139
	v_max3_f32 v132, v132, v136, v140
	s_nop 1
	v_max_f32_dpp v132, v132, v132 quad_perm:[1,0,3,2] row_mask:0xf bank_mask:0xf
	s_nop 1
	v_max_f32_dpp v132, v132, v132 quad_perm:[2,3,0,1] row_mask:0xf bank_mask:0xf
	s_nop 1
	v_max_f32_dpp v132, v132, v132 row_half_mirror row_mask:0xf bank_mask:0xf
	s_nop 1
	v_max_f32_dpp v132, v132, v132 row_mirror row_mask:0xf bank_mask:0xf
	s_nop 1
	v_readlane_b32 s36, v132, 0
	v_readlane_b32 s37, v132, 16
	v_readlane_b32 s38, v132, 32
	v_readlane_b32 s39, v132, 48
	s_nop 2
	v_mov_b32_e32 v133, s36
	v_max_f32_e32 v133, s37, v133
	v_max_f32_e32 v133, s38, v133
	v_max_f32_e32 v133, s39, v133
	s_mov_b32 s37, 0xf800000
	v_mul_f32_e32 v137, 0x4f800000, v133
	v_cmp_gt_f32_e32 vcc, s37, v133
	s_nop 1
	v_cndmask_b32_e32 v133, v133, v137, vcc
	v_sqrt_f32_e32 v137, v133
	s_nop 0
	v_add_u32_e32 v138, -1, v137
	v_add_u32_e32 v139, 1, v137
	v_fma_f32 v143, -v138, v137, v133
	v_fma_f32 v144, -v139, v137, v133
	v_cmp_ge_f32_e64 s[38:39], 0, v143
	s_nop 1
	v_cndmask_b32_e64 v137, v137, v138, s[38:39]
	v_cmp_lt_f32_e64 s[38:39], 0, v144
	s_nop 1
	v_cndmask_b32_e64 v137, v137, v139, s[38:39]
	v_mul_f32_e32 v138, 0x37800000, v137
	v_cndmask_b32_e32 v137, v137, v138, vcc
	v_mov_b32_e32 v138, 0x260
	v_cmp_class_f32_e32 vcc, v133, v138
	s_nop 1
	v_cndmask_b32_e32 v133, v137, v133, vcc
	v_mov_b32_e32 v135, 0x3ca3d70a
	s_mov_b32 s36, 0xffff
	v_mul_f32_e32 v134, v141, v133
	v_mul_f32_e32 v136, v142, v133
	v_fmamk_f32 v134, v134, 0x3f804189, v135
	v_fmamk_f32 v136, v136, 0x3f804189, v135
	v_cvt_f16_f32_e64 v134, -v134
	v_cvt_f16_f32_e64 v136, -v136
	v_cmp_gt_u32_e32 vcc, 32, v1
	v_cvt_f32_f16_e32 v148, v134
	v_cvt_f32_f16_e32 v149, v136
	v_bfi_b32 v134, s36, v134, v11
	v_bfi_b32 v136, s36, v136, v15
	v_cndmask_b32_e32 v11, v11, v134, vcc
	v_cndmask_b32_e32 v15, v15, v136, vcc
	s_waitcnt vmcnt(0)
	s_barrier
	s_mov_b32 s28, 2
	v_add_u32_e32 v128, s46, v2
	v_add_u32_e32 v129, s47, v2
	ds_read_b128 v[88:91], v128 offset:24576
	ds_read_b128 v[92:95], v128 offset:25600
	ds_read_b128 v[96:99], v128 offset:0
	ds_read_b128 v[104:107], v128 offset:2048
	ds_read_b128 v[100:103], v128 offset:1024
	ds_read_b128 v[108:111], v128 offset:3072
	s_sub_u32 s30, s28, s25
	s_mul_i32 s30, s30, 6
	s_add_u32 s30, s30, s24
	s_mul_i32 s31, s28, 6
	s_add_u32 s31, s31, s22
	s_cmp_lt_u32 s28, s25
	s_cselect_b32 s30, s31, s30
	s_lshl_b32 s33, s18, 10
	s_lshl_b32 s31, s30, 12
	s_add_u32 s31, s31, s33
	s_add_u32 s50, s8, s31
	s_addc_u32 s51, s9, 0
	s_add_u32 s52, s50, 0x3000
	s_addc_u32 s53, s51, 0
	s_add_u32 s34, s48, s33
	s_mov_b32 m0, s34
	s_add_u32 s35, s34, 0x3000
	global_load_lds_dwordx4 v2, s[50:51]
	s_mov_b32 m0, s35
	s_nop 0
	global_load_lds_dwordx4 v2, s[52:53]
	s_cmp_lt_u32 s18, 6
	s_cbranch_scc0 .Lm_nok_p2
	s_lshl_b32 s31, s30, 10
	s_add_u32 s31, s31, s33
	s_add_u32 s54, s4, s31
	s_addc_u32 s55, s5, 0
	s_add_u32 s34, s34, 24576
	s_mov_b32 m0, s34
	s_nop 0
	global_load_lds_dwordx4 v2, s[54:55]
.Lm_nok_p2:
	s_waitcnt lgkmcnt(5)
	v_mfma_f32_32x32x16_f16 v[48:63], v[88:91], v[8:11], 0
	s_nop 5
	s_waitcnt lgkmcnt(4)
	v_mfma_f32_32x32x16_f16 v[64:79], v[92:95], v[8:11], 0
	ds_read_b128 v[88:91], v128 offset:26624
	ds_read_b128 v[112:115], v128 offset:4096
	ds_read_b128 v[120:123], v128 offset:6144
	v_exp_f32_e32 v48, v48
	v_exp_f32_e32 v49, v49
	v_exp_f32_e32 v50, v50
	v_exp_f32_e32 v51, v51
	v_exp_f32_e32 v52, v52
	v_exp_f32_e32 v53, v53
	v_exp_f32_e32 v54, v54
	v_exp_f32_e32 v55, v55
	v_cvt_pk_bf16_f32 v80, v48, v49
	v_cvt_pk_bf16_f32 v81, v50, v51
	v_cvt_pk_bf16_f32 v82, v52, v53
	v_cvt_pk_bf16_f32 v83, v54, v55
	ds_read_b128 v[116:119], v128 offset:5120
	ds_read_b128 v[124:127], v128 offset:7168
	v_exp_f32_e32 v56, v56
	v_exp_f32_e32 v57, v57
	v_exp_f32_e32 v58, v58
	v_exp_f32_e32 v59, v59
	s_waitcnt lgkmcnt(7)
	v_mfma_f32_32x32x16_bf16 v[16:31], v[96:99], v[80:83], 0
	v_exp_f32_e32 v60, v60
	v_exp_f32_e32 v61, v61
	v_exp_f32_e32 v62, v62
	v_exp_f32_e32 v63, v63
	v_mfma_f32_32x32x16_bf16 v[32:47], v[104:107], v[80:83], 0
	v_cvt_pk_bf16_f32 v84, v56, v57
	v_cvt_pk_bf16_f32 v85, v58, v59
	v_cvt_pk_bf16_f32 v86, v60, v61
	v_cvt_pk_bf16_f32 v87, v62, v63
	s_branch .Lm_steps1
